# g2p without the MLA static priority raise (A/B: raise vs none)
# baseline (speedup 1.0000x reference)
; #define PHASE_LOCALS unsigned long long wsu_ = (unsigned long long)ws0; asm volatile("" : "+s"(wsu_)); unsigned char* ws = (unsigned char*)(GAS unsigned char*)wsu_; unsigned long long xou_ = (unsigned long long)xo0; asm volatile("" : "+s"(xou_)); float* xo = (float*)(GAS float*)xou_; BODY_LOCALS
; __global__ void __launch_bounds__(NWAVES * 64, 2) fwd_kernel(Args args) {
;     ...
;         if (((PHASE_MASK >> 5) & 1) && IN(P + 5)) for (int rep_ = 0; rep_ < 1 + ((PHASE_TWICE >> 5) & 1); ++rep_) { PHASE_LOCALS
;             { BODY_LOCALS mla_attn_phase(ring, WSP(WS_MLAQ), MLAKV_D, WSP(WS_ZABC), WSP(WS_OABC), ((float*)(ws + WS_ROPE)), ((float*)(ws + WS_ROPE) + SEQ * 32), vcu, G, tid); }
.LBB0_1119:
	v_readlane_b32 s12, v252, 6
	v_readlane_b32 s8, v252, 4
	v_readlane_b32 s18, v252, 12
	v_readlane_b32 s19, v252, 13
	v_readlane_b32 s9, v252, 5
	s_mov_b64 s[6:7], s[18:19]
	v_mbcnt_lo_u32_b32 v0, -1, 0
	v_mbcnt_hi_u32_b32 v0, -1, v0
	v_readlane_b32 s0, v252, 37
	s_nop 3
	s_cmpk_lt_u32 s0, 0x100
	s_cbranch_scc1 .Lmla_prio_done
	s_setprio 0
